# baseline (speedup 1.0000x reference)
_Z8k2_fusedPKDF16_PKDv8_DF16_PKfS5_S5_PfPiS6_:
	s_lshl_b32 s3, s2, 2
	s_ashr_i32 s16, s2, 4
	s_and_b32 s12, s3, 48
	s_lshl_b32 s2, s2, 4
	s_and_b32 s13, s2, 48
	s_add_i32 s2, s12, -2
	v_mul_u32_u24_e32 v1, 0x334, v0
	s_movk_i32 s15, 0xffec
	s_add_i32 s3, s13, -2
	v_lshrrev_b32_e32 v84, 2, v0
	v_mul_i32_i24_sdwa v2, v1, s15 dst_sel:DWORD dst_unused:UNUSED_PAD src0_sel:WORD_1 src1_sel:DWORD
	v_add_u32_sdwa v48, s2, v1 dst_sel:DWORD dst_unused:UNUSED_PAD src0_sel:DWORD src1_sel:WORD_1
	s_load_dwordx8 s[4:11], s[0:1], 0x0
	s_load_dwordx4 s[32:35], s[0:1], 0x20
	s_load_dwordx2 s[36:37], s[0:1], 0x38
	v_add3_u32 v49, s3, v84, v2
	v_max_i32_e32 v1, 0, v48
	s_lshl_b32 s14, s16, 12
	v_med3_i32 v2, v49, 0, 63
	v_lshlrev_b32_e32 v1, 6, v1
	v_or3_b32 v1, v1, v2, s14
	v_lshlrev_b32_e32 v2, 5, v1
	v_ashrrev_i32_e32 v3, 31, v2
	v_lshlrev_b32_e32 v85, 4, v0
	s_waitcnt lgkmcnt(0)
	v_lshl_add_u64 v[2:3], v[2:3], 1, s[4:5]
	v_and_b32_e32 v46, 48, v85
	v_mov_b32_e32 v47, 0
	v_or_b32_e32 v54, 0x200, v0
	v_lshl_add_u64 v[2:3], v[2:3], 0, v[46:47]
	v_mul_u32_u24_e32 v1, 0x334, v54
	global_load_dwordx4 v[18:21], v[2:3], off
	v_lshrrev_b32_e32 v86, 2, v54
	v_mul_i32_i24_sdwa v2, v1, s15 dst_sel:DWORD dst_unused:UNUSED_PAD src0_sel:WORD_1 src1_sel:DWORD
	v_add_u32_sdwa v50, s2, v1 dst_sel:DWORD dst_unused:UNUSED_PAD src0_sel:DWORD src1_sel:WORD_1
	v_add3_u32 v51, s3, v86, v2
	v_min_u32_e32 v1, 63, v50
	v_med3_i32 v2, v51, 0, 63
	v_lshlrev_b32_e32 v1, 6, v1
	v_or3_b32 v1, v1, v2, s14
	v_lshlrev_b32_e32 v2, 5, v1
	v_or_b32_e32 v58, 0x400, v0
	v_ashrrev_i32_e32 v3, 31, v2
	v_lshlrev_b32_e32 v87, 4, v54
	v_mul_u32_u24_e32 v1, 0x667, v58
	v_lshl_add_u64 v[2:3], v[2:3], 1, s[4:5]
	v_and_b32_e32 v4, 48, v87
	v_mov_b32_e32 v5, v47
	v_lshrrev_b32_e32 v1, 17, v1
	v_lshl_add_u64 v[2:3], v[2:3], 0, v[4:5]
	v_mul_i32_i24_e32 v4, 0xffffffec, v1
	v_add_u32_e32 v52, s2, v1
	v_lshrrev_b32_e32 v88, 2, v58
	v_add3_u32 v53, s3, v88, v4
	v_min_u32_e32 v1, 63, v52
	v_med3_i32 v4, v53, 0, 63
	v_lshlrev_b32_e32 v1, 6, v1
	v_or3_b32 v1, v1, v4, s14
	v_lshlrev_b32_e32 v4, 5, v1
	v_ashrrev_i32_e32 v5, 31, v4
	v_or_b32_e32 v89, 0x600, v0
	v_lshl_add_u64 v[4:5], v[4:5], 1, s[4:5]
	v_min_u32_e32 v1, 0x63f, v89
	v_lshl_add_u64 v[4:5], v[4:5], 0, v[46:47]
	global_load_dwordx4 v[22:25], v[2:3], off
	global_load_dwordx4 v[26:29], v[4:5], off
	v_lshrrev_b32_e32 v2, 2, v1
	v_add_u32_e32 v2, s3, v2
	s_add_i32 s15, s12, 17
	v_add_u32_e32 v55, 0xfffffe84, v2
	s_min_u32 s2, s15, 63
	v_min_u32_e32 v2, 63, v55
	v_lshl_or_b32 v2, s2, 6, v2
	v_or_b32_e32 v2, s14, v2
	v_lshlrev_b32_e32 v2, 5, v2
	v_ashrrev_i32_e32 v3, 31, v2
	v_lshlrev_b32_e32 v1, 4, v1
	v_lshl_add_u64 v[2:3], v[2:3], 1, s[4:5]
	v_and_b32_e32 v4, 48, v1
	v_mov_b32_e32 v5, v47
	v_min_u32_e32 v1, 0x47f, v58
	v_lshrrev_b32_e32 v164, 1, v0
	v_lshl_add_u64 v[2:3], v[2:3], 0, v[4:5]
	v_lshlrev_b32_e32 v90, 4, v1
	v_and_b32_e32 v162, 16, v164
	global_load_dwordx4 v[30:33], v[2:3], off
	global_load_dwordx4 v[34:37], v85, s[6:7]
	global_load_dwordx4 v[38:41], v87, s[6:7]
	global_load_dwordx4 v[42:45], v90, s[6:7]
	s_nop 0
	global_load_dwordx4 v[2:5], v162, s[8:9]
	global_load_dwordx4 v[6:9], v162, s[8:9] offset:32
	global_load_dwordx4 v[10:13], v162, s[8:9] offset:64
	global_load_dwordx4 v[14:17], v162, s[8:9] offset:96
	v_or_b32_e32 v48, v48, v49
	v_cmp_gt_u32_e32 vcc, 64, v48
	v_or_b32_e32 v48, v50, v51
	v_cmp_gt_u32_e64 s[2:3], 64, v48
	v_or_b32_e32 v48, v52, v53
	v_and_b32_e32 v1, 63, v0
	v_and_b32_e32 v165, 31, v0
	v_cmp_gt_u32_e64 s[4:5], 64, v48
	v_or_b32_e32 v48, s15, v55
	v_lshrrev_b32_e32 v163, 6, v0
	v_cmp_gt_u32_e64 s[6:7], 64, v48
	s_movk_i32 s8, 0x50
	s_waitcnt vmcnt(10)
	v_cndmask_b32_e32 v19, 0, v19, vcc
	v_cndmask_b32_e32 v18, 0, v18, vcc
	v_cndmask_b32_e32 v21, 0, v21, vcc
	v_cndmask_b32_e32 v20, 0, v20, vcc
	v_mad_u32_u24 v47, v84, s8, v46
	ds_write_b128 v47, v[18:21]
	s_waitcnt vmcnt(9)
	v_cndmask_b32_e64 v19, 0, v23, s[2:3]
	v_cndmask_b32_e64 v18, 0, v22, s[2:3]
	v_cndmask_b32_e64 v21, 0, v25, s[2:3]
	v_cndmask_b32_e64 v20, 0, v24, s[2:3]
	v_mad_u32_u24 v22, v86, s8, v46
	ds_write_b128 v22, v[18:21]
	s_waitcnt vmcnt(8)
	v_cndmask_b32_e64 v19, 0, v27, s[4:5]
	v_cndmask_b32_e64 v18, 0, v26, s[4:5]
	v_cndmask_b32_e64 v21, 0, v29, s[4:5]
	v_cndmask_b32_e64 v20, 0, v28, s[4:5]
	v_mad_u32_u24 v22, v88, s8, v46
	ds_write_b128 v22, v[18:21]
	v_lshrrev_b32_e32 v22, 2, v89
	s_waitcnt vmcnt(7)
	v_cndmask_b32_e64 v19, 0, v31, s[6:7]
	v_cndmask_b32_e64 v18, 0, v30, s[6:7]
	v_cndmask_b32_e64 v21, 0, v33, s[6:7]
	v_cndmask_b32_e64 v20, 0, v32, s[6:7]
	v_mad_u32_u24 v22, v22, s8, v46
	ds_write_b128 v22, v[18:21]
	s_waitcnt vmcnt(6)
	ds_write_b128 v85, v[34:37] offset:57920
	s_waitcnt vmcnt(5)
	ds_write_b128 v87, v[38:41] offset:57920
	s_waitcnt vmcnt(4)
	ds_write_b128 v90, v[42:45] offset:57920
	v_lshlrev_b32_e32 v18, 4, v1
	s_waitcnt lgkmcnt(0)
	s_barrier
	s_lshr_b32 s27, s12, 1
	s_lshr_b32 s26, s13, 1
	v_add_u32_e32 v48, s27, v163
	v_bfe_u32 v49, v0, 1, 3
	v_add_u32_e32 v49, s26, v49
	v_lshlrev_b32_e32 v48, 10, v48
	v_lshl_or_b32 v48, v49, 5, v48
	v_bfe_u32 v49, v0, 5, 1
	v_lshl_or_b32 v48, v49, 2, v48
	v_bfe_u32 v49, v0, 4, 1
	v_lshl_or_b32 v48, v49, 1, v48
	v_and_b32_e32 v49, 1, v0
	v_or_b32_e32 v48, v48, v49
	v_mul_u32_u24_e32 v210, 40, v48
	v_add_u32_e32 v19, 0xe240, v18
	ds_read_b128 v[150:153], v18 offset:57920
	ds_read_b128 v[146:149], v18 offset:58944
	ds_read_b128 v[142:145], v18 offset:59968
	ds_read_b128 v[138:141], v18 offset:60992
	ds_read_b128 v[134:137], v18 offset:62016
	ds_read_b128 v[130:133], v18 offset:63040
	ds_read_b128 v[126:129], v18 offset:64064
	ds_read_b128 v[122:125], v18 offset:65088
	ds_read_b128 v[118:121], v19 offset:8192
	ds_read_b128 v[114:117], v19 offset:9216
	ds_read_b128 v[110:113], v19 offset:10240
	ds_read_b128 v[106:109], v19 offset:11264
	ds_read_b128 v[102:105], v19 offset:12288
	ds_read_b128 v[98:101], v19 offset:13312
	ds_read_b128 v[94:97], v19 offset:14336
	ds_read_b128 v[90:93], v19 offset:15360
	ds_read_b128 v[86:89], v19 offset:16384
	ds_read_b128 v[82:85], v19 offset:17408
	v_lshl_or_b32 v166, v163, 5, v165
	v_mul_u32_u24_e32 v18, 0xe39, v166
	v_lshrrev_b32_e32 v168, 16, v18
	s_movk_i32 s4, 0xffee
	v_mad_i32_i24 v169, v168, s4, v166
	v_min_u32_e32 v19, 0x43, v166
	v_mad_u32_u24 v18, v168, 20, v169
	v_or_b32_e32 v165, 0x100, v19
	s_movk_i32 s2, 0xc0
	v_mul_lo_u32 v18, v18, s8
	v_mul_u32_u24_e32 v19, 0xe39, v165
	v_cmp_gt_u32_e32 vcc, s2, v0
	s_movk_i32 s2, 0xbf
	v_lshrrev_b32_e32 v167, 16, v19
	v_cmp_lt_u32_e64 s[2:3], s2, v0
	v_add_u32_e32 v171, v18, v162
	s_and_saveexec_b64 s[6:7], s[2:3]
	s_xor_b64 s[2:3], exec, s[6:7]
	s_cbranch_execz .LBB1_2
	ds_read_b128 v[34:37], v171
	ds_read_b128 v[38:41], v171 offset:32
	ds_read_b128 v[42:45], v171 offset:80
	ds_read_b128 v[46:49], v171 offset:112
	ds_read_b128 v[172:175], v171 offset:160
	ds_read_b128 v[176:179], v171 offset:192
	ds_read_b128 v[180:183], v171 offset:1600
	ds_read_b128 v[184:187], v171 offset:1632
	ds_read_b128 v[188:191], v171 offset:1680
	s_waitcnt vmcnt(0) lgkmcnt(8)
	v_mfma_f32_32x32x16_f16 v[18:33], v[150:153], v[34:37], v[2:17]
	s_waitcnt lgkmcnt(7)
	v_mfma_f32_32x32x16_f16 v[18:33], v[146:149], v[38:41], v[18:33]
	ds_read_b128 v[34:37], v171 offset:1712
	s_waitcnt lgkmcnt(7)
	v_mfma_f32_32x32x16_f16 v[18:33], v[142:145], v[42:45], v[18:33]
	ds_read_b128 v[38:41], v171 offset:1760
	global_load_dwordx4 v[66:69], v210, s[10:11]
	s_waitcnt lgkmcnt(7)
	v_mfma_f32_32x32x16_f16 v[18:33], v[138:141], v[46:49], v[18:33]
	ds_read_b128 v[42:45], v171 offset:1792
	global_load_dwordx4 v[50:53], v210, s[10:11] offset:16
	s_waitcnt lgkmcnt(7)
	v_mfma_f32_32x32x16_f16 v[18:33], v[134:137], v[172:175], v[18:33]
	ds_read_b128 v[46:49], v171 offset:3200
	global_load_dwordx2 v[156:157], v210, s[10:11] offset:32
	s_waitcnt lgkmcnt(7)
	v_mfma_f32_32x32x16_f16 v[18:33], v[130:133], v[176:179], v[18:33]
	ds_read_b128 v[172:175], v171 offset:3232
	global_load_dwordx4 v[70:73], v210, s[10:11] offset:320
	s_waitcnt lgkmcnt(7)
	v_mfma_f32_32x32x16_f16 v[18:33], v[126:129], v[180:183], v[18:33]
	ds_read_b128 v[176:179], v171 offset:3280
	global_load_dwordx4 v[54:57], v210, s[10:11] offset:336
	s_waitcnt lgkmcnt(7)
	v_mfma_f32_32x32x16_f16 v[18:33], v[122:125], v[184:187], v[18:33]
	ds_read_b128 v[180:183], v171 offset:3312
	global_load_dwordx2 v[154:155], v210, s[10:11] offset:352
	s_waitcnt lgkmcnt(7)
	v_mfma_f32_32x32x16_f16 v[18:33], v[118:121], v[188:191], v[18:33]
	ds_read_b128 v[184:187], v171 offset:3360
	global_load_dwordx4 v[74:77], v210, s[10:11] offset:640
	s_waitcnt lgkmcnt(7)
	v_mfma_f32_32x32x16_f16 v[18:33], v[114:117], v[34:37], v[18:33]
	ds_read_b128 v[188:191], v171 offset:3392
	global_load_dwordx4 v[58:61], v210, s[10:11] offset:656
	s_waitcnt lgkmcnt(7)
	v_mfma_f32_32x32x16_f16 v[18:33], v[110:113], v[38:41], v[18:33]
	global_load_dwordx2 v[160:161], v210, s[10:11] offset:672
	s_waitcnt lgkmcnt(6)
	v_mfma_f32_32x32x16_f16 v[18:33], v[106:109], v[42:45], v[18:33]
	global_load_dwordx4 v[78:81], v210, s[10:11] offset:960
	s_waitcnt lgkmcnt(5)
	v_mfma_f32_32x32x16_f16 v[18:33], v[102:105], v[46:49], v[18:33]
	global_load_dwordx4 v[62:65], v210, s[10:11] offset:976
	s_waitcnt lgkmcnt(4)
	v_mfma_f32_32x32x16_f16 v[18:33], v[98:101], v[172:175], v[18:33]
	global_load_dwordx2 v[158:159], v210, s[10:11] offset:992
	s_waitcnt lgkmcnt(3)
	v_mfma_f32_32x32x16_f16 v[18:33], v[94:97], v[176:179], v[18:33]
	s_waitcnt lgkmcnt(2)
	v_mfma_f32_32x32x16_f16 v[18:33], v[90:93], v[180:183], v[18:33]
	s_waitcnt lgkmcnt(1)
	v_mfma_f32_32x32x16_f16 v[18:33], v[86:89], v[184:187], v[18:33]
	s_waitcnt lgkmcnt(0)
	v_mfma_f32_32x32x16_f16 v[18:33], v[82:85], v[188:191], v[18:33]
	v_mov_b32_e32 v49, v17
	v_mov_b32_e32 v48, v16
	v_mov_b32_e32 v47, v15
	v_mov_b32_e32 v46, v14
	v_mov_b32_e32 v45, v13
	v_mov_b32_e32 v44, v12
	v_mov_b32_e32 v43, v11
	v_mov_b32_e32 v42, v10
	v_mov_b32_e32 v41, v9
	v_mov_b32_e32 v40, v8
	v_mov_b32_e32 v39, v7
	v_mov_b32_e32 v38, v6
	v_mov_b32_e32 v37, v5
	v_mov_b32_e32 v36, v4
	v_mov_b32_e32 v35, v3
	v_mov_b32_e32 v34, v2
.LBB1_2:
	s_or_saveexec_b64 s[2:3], s[2:3]
	v_mad_i32_i24 v170, v167, s4, v165
	s_xor_b64 exec, exec, s[2:3]
	s_cbranch_execz .LBB1_4
	v_mad_u32_u24 v18, v167, 20, v170
	s_movk_i32 s4, 0x50
	v_mad_u64_u32 v[208:209], s[4:5], v18, s4, v[162:163]
	ds_read_b128 v[34:37], v171
	ds_read_b128 v[38:41], v171 offset:32
	ds_read_b128 v[42:45], v171 offset:80
	ds_read_b128 v[46:49], v171 offset:112
	ds_read_b128 v[172:175], v171 offset:160
	ds_read_b128 v[176:179], v171 offset:192
	ds_read_b128 v[180:183], v171 offset:1600
	ds_read_b128 v[184:187], v171 offset:1632
	ds_read_b128 v[188:191], v171 offset:1680
	s_waitcnt vmcnt(0) lgkmcnt(8)
	v_mfma_f32_32x32x16_f16 v[18:33], v[150:153], v[34:37], v[2:17]
	s_waitcnt lgkmcnt(7)
	v_mfma_f32_32x32x16_f16 v[18:33], v[146:149], v[38:41], v[18:33]
	ds_read_b128 v[34:37], v171 offset:1712
	s_waitcnt lgkmcnt(7)
	v_mfma_f32_32x32x16_f16 v[18:33], v[142:145], v[42:45], v[18:33]
	ds_read_b128 v[38:41], v171 offset:1760
	global_load_dwordx4 v[66:69], v210, s[10:11]
	s_waitcnt lgkmcnt(7)
	v_mfma_f32_32x32x16_f16 v[18:33], v[138:141], v[46:49], v[18:33]
	ds_read_b128 v[42:45], v171 offset:1792
	global_load_dwordx4 v[50:53], v210, s[10:11] offset:16
	s_waitcnt lgkmcnt(7)
	v_mfma_f32_32x32x16_f16 v[18:33], v[134:137], v[172:175], v[18:33]
	ds_read_b128 v[46:49], v171 offset:3200
	global_load_dwordx2 v[156:157], v210, s[10:11] offset:32
	s_waitcnt lgkmcnt(7)
	v_mfma_f32_32x32x16_f16 v[18:33], v[130:133], v[176:179], v[18:33]
	ds_read_b128 v[172:175], v171 offset:3232
	global_load_dwordx4 v[70:73], v210, s[10:11] offset:320
	s_waitcnt lgkmcnt(7)
	v_mfma_f32_32x32x16_f16 v[18:33], v[126:129], v[180:183], v[18:33]
	ds_read_b128 v[176:179], v171 offset:3280
	global_load_dwordx4 v[54:57], v210, s[10:11] offset:336
	s_waitcnt lgkmcnt(7)
	v_mfma_f32_32x32x16_f16 v[18:33], v[122:125], v[184:187], v[18:33]
	ds_read_b128 v[180:183], v171 offset:3312
	global_load_dwordx2 v[154:155], v210, s[10:11] offset:352
	s_waitcnt lgkmcnt(7)
	v_mfma_f32_32x32x16_f16 v[18:33], v[118:121], v[188:191], v[18:33]
	ds_read_b128 v[184:187], v171 offset:3360
	global_load_dwordx4 v[74:77], v210, s[10:11] offset:640
	s_waitcnt lgkmcnt(7)
	v_mfma_f32_32x32x16_f16 v[18:33], v[114:117], v[34:37], v[18:33]
	ds_read_b128 v[188:191], v171 offset:3392
	global_load_dwordx4 v[58:61], v210, s[10:11] offset:656
	s_waitcnt lgkmcnt(7)
	v_mfma_f32_32x32x16_f16 v[18:33], v[110:113], v[38:41], v[18:33]
	ds_read_b128 v[192:195], v208
	global_load_dwordx2 v[160:161], v210, s[10:11] offset:672
	s_waitcnt lgkmcnt(7)
	v_mfma_f32_32x32x16_f16 v[18:33], v[106:109], v[42:45], v[18:33]
	ds_read_b128 v[196:199], v208 offset:32
	global_load_dwordx4 v[78:81], v210, s[10:11] offset:960
	s_waitcnt lgkmcnt(7)
	v_mfma_f32_32x32x16_f16 v[18:33], v[102:105], v[46:49], v[18:33]
	ds_read_b128 v[200:203], v208 offset:80
	global_load_dwordx4 v[62:65], v210, s[10:11] offset:976
	s_waitcnt lgkmcnt(7)
	v_mfma_f32_32x32x16_f16 v[18:33], v[98:101], v[172:175], v[18:33]
	ds_read_b128 v[204:207], v208 offset:112
	global_load_dwordx2 v[158:159], v210, s[10:11] offset:992
	s_waitcnt lgkmcnt(7)
	v_mfma_f32_32x32x16_f16 v[18:33], v[94:97], v[176:179], v[18:33]
	ds_read_b128 v[172:175], v208 offset:160
	s_waitcnt lgkmcnt(7)
	v_mfma_f32_32x32x16_f16 v[18:33], v[90:93], v[180:183], v[18:33]
	ds_read_b128 v[176:179], v208 offset:192
	s_waitcnt lgkmcnt(7)
	v_mfma_f32_32x32x16_f16 v[18:33], v[86:89], v[184:187], v[18:33]
	ds_read_b128 v[180:183], v208 offset:1600
	s_waitcnt lgkmcnt(7)
	v_mfma_f32_32x32x16_f16 v[18:33], v[82:85], v[188:191], v[18:33]
	ds_read_b128 v[184:187], v208 offset:1632
	s_waitcnt lgkmcnt(7)
	v_mfma_f32_32x32x16_f16 v[34:49], v[150:153], v[192:195], v[2:17]
	ds_read_b128 v[188:191], v208 offset:1680
	s_waitcnt lgkmcnt(7)
	v_mfma_f32_32x32x16_f16 v[34:49], v[146:149], v[196:199], v[34:49]
	ds_read_b128 v[192:195], v208 offset:1712
	s_waitcnt lgkmcnt(7)
	v_mfma_f32_32x32x16_f16 v[34:49], v[142:145], v[200:203], v[34:49]
	ds_read_b128 v[196:199], v208 offset:1760
	s_waitcnt lgkmcnt(7)
	v_mfma_f32_32x32x16_f16 v[34:49], v[138:141], v[204:207], v[34:49]
	ds_read_b128 v[200:203], v208 offset:1792
	s_waitcnt lgkmcnt(7)
	v_mfma_f32_32x32x16_f16 v[34:49], v[134:137], v[172:175], v[34:49]
	ds_read_b128 v[204:207], v208 offset:3200
	s_waitcnt lgkmcnt(7)
	v_mfma_f32_32x32x16_f16 v[34:49], v[130:133], v[176:179], v[34:49]
	ds_read_b128 v[172:175], v208 offset:3232
	s_waitcnt lgkmcnt(7)
	v_mfma_f32_32x32x16_f16 v[34:49], v[126:129], v[180:183], v[34:49]
	ds_read_b128 v[176:179], v208 offset:3280
	s_waitcnt lgkmcnt(7)
	v_mfma_f32_32x32x16_f16 v[34:49], v[122:125], v[184:187], v[34:49]
	ds_read_b128 v[180:183], v208 offset:3312
	s_waitcnt lgkmcnt(7)
	v_mfma_f32_32x32x16_f16 v[34:49], v[118:121], v[188:191], v[34:49]
	ds_read_b128 v[184:187], v208 offset:3360
	s_waitcnt lgkmcnt(7)
	v_mfma_f32_32x32x16_f16 v[34:49], v[114:117], v[192:195], v[34:49]
	ds_read_b128 v[188:191], v208 offset:3392
	s_waitcnt lgkmcnt(7)
	v_mfma_f32_32x32x16_f16 v[34:49], v[110:113], v[196:199], v[34:49]
	s_waitcnt lgkmcnt(6)
	v_mfma_f32_32x32x16_f16 v[34:49], v[106:109], v[200:203], v[34:49]
	s_waitcnt lgkmcnt(5)
	v_mfma_f32_32x32x16_f16 v[34:49], v[102:105], v[204:207], v[34:49]
	s_waitcnt lgkmcnt(4)
	v_mfma_f32_32x32x16_f16 v[34:49], v[98:101], v[172:175], v[34:49]
	s_waitcnt lgkmcnt(3)
	v_mfma_f32_32x32x16_f16 v[34:49], v[94:97], v[176:179], v[34:49]
	s_waitcnt lgkmcnt(2)
	v_mfma_f32_32x32x16_f16 v[34:49], v[90:93], v[180:183], v[34:49]
	s_waitcnt lgkmcnt(1)
	v_mfma_f32_32x32x16_f16 v[34:49], v[86:89], v[184:187], v[34:49]
	s_waitcnt lgkmcnt(0)
	v_mfma_f32_32x32x16_f16 v[34:49], v[82:85], v[188:191], v[34:49]

	.amdhsa_kernel _Z8k2_fusedPKDF16_PKDv8_DF16_PKfS5_S5_PfPiS6_
		.amdhsa_group_segment_fixed_size 85824
		.amdhsa_private_segment_fixed_size 0
		.amdhsa_kernarg_size 64
		.amdhsa_user_sgpr_count 2
		.amdhsa_user_sgpr_dispatch_ptr 0
		.amdhsa_user_sgpr_queue_ptr 0
		.amdhsa_user_sgpr_kernarg_segment_ptr 1
		.amdhsa_user_sgpr_dispatch_id 0
		.amdhsa_user_sgpr_kernarg_preload_length 0
		.amdhsa_user_sgpr_kernarg_preload_offset 0
		.amdhsa_user_sgpr_private_segment_size 0
		.amdhsa_uses_dynamic_stack 0
		.amdhsa_enable_private_segment 0
		.amdhsa_system_sgpr_workgroup_id_x 1
		.amdhsa_system_sgpr_workgroup_id_y 0
		.amdhsa_system_sgpr_workgroup_id_z 0
		.amdhsa_system_sgpr_workgroup_info 0
		.amdhsa_system_vgpr_workitem_id 0
		.amdhsa_next_free_vgpr 212
		.amdhsa_next_free_sgpr 96
		.amdhsa_accum_offset 212
		.amdhsa_reserve_vcc 1
		.amdhsa_float_round_mode_32 0
		.amdhsa_float_round_mode_16_64 0
		.amdhsa_float_denorm_mode_32 3
		.amdhsa_float_denorm_mode_16_64 3
		.amdhsa_dx10_clamp 1
		.amdhsa_ieee_mode 1
		.amdhsa_fp16_overflow 0
		.amdhsa_tg_split 0
		.amdhsa_exception_fp_ieee_invalid_op 0
		.amdhsa_exception_fp_denorm_src 0
		.amdhsa_exception_fp_ieee_div_zero 0
		.amdhsa_exception_fp_ieee_overflow 0
		.amdhsa_exception_fp_ieee_underflow 0
		.amdhsa_exception_fp_ieee_inexact 0
		.amdhsa_exception_int_div_zero 0
	.end_amdhsa_kernel

.Lfunc_end1:
	.size	_Z8k2_fusedPKDF16_PKDv8_DF16_PKfS5_S5_PfPiS6_, .Lfunc_end1-_Z8k2_fusedPKDF16_PKDv8_DF16_PKfS5_S5_PfPiS6_
	.set _Z8k2_fusedPKDF16_PKDv8_DF16_PKfS5_S5_PfPiS6_.num_vgpr, 212
	.set _Z8k2_fusedPKDF16_PKDv8_DF16_PKfS5_S5_PfPiS6_.num_agpr, 0
	.set _Z8k2_fusedPKDF16_PKDv8_DF16_PKfS5_S5_PfPiS6_.numbered_sgpr, 26
	.set _Z8k2_fusedPKDF16_PKDv8_DF16_PKfS5_S5_PfPiS6_.num_named_barrier, 0
	.set _Z8k2_fusedPKDF16_PKDv8_DF16_PKfS5_S5_PfPiS6_.private_seg_size, 0
	.set _Z8k2_fusedPKDF16_PKDv8_DF16_PKfS5_S5_PfPiS6_.uses_vcc, 1
	.set _Z8k2_fusedPKDF16_PKDv8_DF16_PKfS5_S5_PfPiS6_.uses_flat_scratch, 0
	.set _Z8k2_fusedPKDF16_PKDv8_DF16_PKfS5_S5_PfPiS6_.has_dyn_sized_stack, 0
	.set _Z8k2_fusedPKDF16_PKDv8_DF16_PKfS5_S5_PfPiS6_.has_recursion, 0
	.set _Z8k2_fusedPKDF16_PKDv8_DF16_PKfS5_S5_PfPiS6_.has_indirect_call, 0

amdhsa.kernels:
  - .agpr_count:     0
    .args:
      - .actual_access:  read_only
        .address_space:  global
        .offset:         0
        .size:           8
        .value_kind:     global_buffer
      - .actual_access:  read_only
        .address_space:  global
        .offset:         8
        .size:           8
        .value_kind:     global_buffer
      - .actual_access:  read_only
        .address_space:  global
        .offset:         16
        .size:           8
        .value_kind:     global_buffer
      - .actual_access:  read_only
        .address_space:  global
        .offset:         24
        .size:           8
        .value_kind:     global_buffer
      - .actual_access:  read_only
        .address_space:  global
        .offset:         32
        .size:           8
        .value_kind:     global_buffer
      - .actual_access:  write_only
        .address_space:  global
        .offset:         40
        .size:           8
        .value_kind:     global_buffer
      - .actual_access:  write_only
        .address_space:  global
        .offset:         48
        .size:           8
        .value_kind:     global_buffer
      - .actual_access:  write_only
        .address_space:  global
        .offset:         56
        .size:           8
        .value_kind:     global_buffer
      - .actual_access:  write_only
        .address_space:  global
        .offset:         64
        .size:           8
        .value_kind:     global_buffer
    .group_segment_fixed_size: 147456
    .kernarg_segment_align: 8
    .kernarg_segment_size: 72
    .language:       OpenCL C
    .language_version:
      - 2
      - 0
    .max_flat_workgroup_size: 768
    .name:           _Z8k1_fusedPKfS0_S0_S0_S0_PDF16_PfPiPDv8_DF16_
    .private_segment_fixed_size: 0
    .sgpr_count:     32
    .sgpr_spill_count: 0
    .symbol:         _Z8k1_fusedPKfS0_S0_S0_S0_PDF16_PfPiPDv8_DF16_.kd
    .uniform_work_group_size: 1
    .uses_dynamic_stack: false
    .vgpr_count:     168
    .vgpr_spill_count: 0
    .wavefront_size: 64
  - .agpr_count:     0
    .args:
      - .actual_access:  read_only
        .address_space:  global
        .offset:         0
        .size:           8
        .value_kind:     global_buffer
      - .actual_access:  read_only
        .address_space:  global
        .offset:         8
        .size:           8
        .value_kind:     global_buffer
      - .actual_access:  read_only
        .address_space:  global
        .offset:         16
        .size:           8
        .value_kind:     global_buffer
      - .actual_access:  read_only
        .address_space:  global
        .offset:         24
        .size:           8
        .value_kind:     global_buffer
      - .actual_access:  read_only
        .address_space:  global
        .offset:         32
        .size:           8
        .value_kind:     global_buffer
      - .address_space:  global
        .offset:         40
        .size:           8
        .value_kind:     global_buffer
      - .address_space:  global
        .offset:         48
        .size:           8
        .value_kind:     global_buffer
      - .actual_access:  write_only
        .address_space:  global
        .offset:         56
        .size:           8
        .value_kind:     global_buffer
    .group_segment_fixed_size: 85824
    .kernarg_segment_align: 8
    .kernarg_segment_size: 64
    .language:       OpenCL C
    .language_version:
      - 2
      - 0
    .max_flat_workgroup_size: 512
    .name:           _Z8k2_fusedPKDF16_PKDv8_DF16_PKfS5_S5_PfPiS6_
    .private_segment_fixed_size: 0
    .sgpr_count:     32
    .sgpr_spill_count: 0
    .symbol:         _Z8k2_fusedPKDF16_PKDv8_DF16_PKfS5_S5_PfPiS6_.kd
    .uniform_work_group_size: 1
    .uses_dynamic_stack: false
    .vgpr_count:     212
    .vgpr_spill_count: 0
    .wavefront_size: 64
